# mix_unit q/kv norm+rope stages: each chain's gain-vector pieces (offsets 64/128/192) requested together at the chain start into idle registers; their per-piece waits folded into the chain's first wait
# baseline (speedup 1.0000x reference)
.LBB0_400:
	s_or_b64 exec, exec, s[0:1]
	s_ashr_i32 s0, s55, 31
	s_lshr_b32 s0, s0, 24
	s_add_i32 s0, s55, s0
	v_and_b32_e32 v91, 15, v1
	v_ashrrev_i32_e32 v88, 4, v1
	s_ashr_i32 s2, s0, 8
	v_lshlrev_b32_e32 v82, 3, v88
	v_xor_b32_e32 v98, 16, v228
	v_xor_b32_e32 v97, 32, v228
	v_lshlrev_b32_e32 v78, 2, v88
	v_or_b32_e32 v80, s90, v91
	s_mov_b64 s[18:19], -1
	s_cmp_gt_i32 s91, 3
	v_lshlrev_b32_e32 v92, 4, v88
	v_ashrrev_i32_e32 v83, 31, v82
	v_cmp_lt_i32_e64 s[0:1], v98, v96
	v_cmp_lt_i32_e32 vcc, v97, v96
	v_ashrrev_i32_e32 v79, 31, v78
	v_ashrrev_i32_e32 v81, 31, v80
	s_waitcnt lgkmcnt(0)
	s_barrier
	s_cbranch_scc0 .LBB0_402
	s_add_i32 s3, s91, -4
	s_lshl_b32 s80, s3, 7
	s_lshl_b64 s[18:19], s[80:81], 8
	s_add_u32 s18, s28, s18
	s_addc_u32 s19, s29, s19
	v_lshlrev_b32_e32 v114, 8, v91
	v_lshl_add_u64 v[2:3], s[18:19], 0, v[114:115]
	v_lshl_add_u64 v[18:19], v[82:83], 1, v[2:3]
	s_movk_i32 s17, 0x4000
	v_add_co_u32_e64 v20, s[38:39], s17, v18
	s_movk_i32 s17, 0x5000
	s_nop 0
	v_addc_co_u32_e64 v21, s[38:39], 0, v19, s[38:39]
	v_add_co_u32_e64 v22, s[38:39], s17, v18
	s_movk_i32 s17, 0x1000
	s_nop 0
	v_addc_co_u32_e64 v23, s[38:39], 0, v19, s[38:39]
	v_add_co_u32_e64 v24, s[38:39], s17, v18
	s_movk_i32 s17, 0x2000
	s_nop 0
	v_addc_co_u32_e64 v25, s[38:39], 0, v19, s[38:39]
	v_add_co_u32_e64 v60, s[38:39], s17, v18
	v_mul_u32_u24_e32 v4, 0x88, v91
	s_nop 0
	v_addc_co_u32_e64 v61, s[38:39], 0, v19, s[38:39]
	s_movk_i32 s17, 0x6000
	v_lshlrev_b32_e32 v4, 1, v4
	v_add_co_u32_e64 v58, s[38:39], s17, v18
	v_add3_u32 v89, 0, v92, v4
	s_nop 0
	v_addc_co_u32_e64 v59, s[38:39], 0, v19, s[38:39]
	s_movk_i32 s17, 0x7000
	ds_read_b128 v[26:29], v89 offset:12800
	ds_read_b128 v[30:33], v89 offset:17152
	global_load_dwordx4 v[6:9], v[18:19], off
	global_load_dwordx4 v[14:17], v[22:23], off offset:-4096
	global_load_dwordx4 v[34:37], v[60:61], off offset:-4096
	global_load_dwordx4 v[38:41], v[22:23], off
	global_load_dwordx4 v[50:53], v[60:61], off
	v_add_co_u32_e64 v84, s[38:39], s17, v18
	s_movk_i32 s17, 0x3000
	s_nop 0
	v_addc_co_u32_e64 v85, s[38:39], 0, v19, s[38:39]
	v_add_co_u32_e64 v86, s[38:39], s17, v18
	global_load_dwordx4 v[54:57], v[84:85], off offset:-4096
	s_nop 0
	v_addc_co_u32_e64 v87, s[38:39], 0, v19, s[38:39]
	global_load_dwordx4 v[70:73], v[86:87], off
	global_load_dwordx4 v[74:77], v[84:85], off
	global_load_dwordx4 v[140:143], v[18:19], off offset:64
	global_load_dwordx4 v[144:147], v[20:21], off offset:64
	global_load_dwordx4 v[148:151], v[24:25], off offset:64
	global_load_dwordx4 v[152:155], v[22:23], off offset:64
	global_load_dwordx4 v[156:159], v[60:61], off offset:64
	global_load_dwordx4 v[160:163], v[58:59], off offset:64
	global_load_dwordx4 v[164:167], v[86:87], off offset:64
	global_load_dwordx4 v[168:171], v[84:85], off offset:64
	global_load_dwordx4 v[172:175], v[18:19], off offset:128
	global_load_dwordx4 v[176:179], v[20:21], off offset:128
	global_load_dwordx4 v[180:183], v[24:25], off offset:128
	global_load_dwordx4 v[184:187], v[22:23], off offset:128
	global_load_dwordx4 v[188:191], v[60:61], off offset:128
	global_load_dwordx4 v[192:195], v[58:59], off offset:128
	global_load_dwordx4 v[196:199], v[86:87], off offset:128
	global_load_dwordx4 v[200:203], v[84:85], off offset:128
	global_load_dwordx4 v[204:207], v[18:19], off offset:192
	global_load_dwordx4 v[208:211], v[20:21], off offset:192
	global_load_dwordx4 v[212:215], v[24:25], off offset:192
	global_load_dwordx4 v[216:219], v[22:23], off offset:192
	global_load_dwordx4 v[220:223], v[60:61], off offset:192
	global_load_dwordx4 v[234:237], v[58:59], off offset:192
	global_load_dwordx4 v[238:241], v[86:87], off offset:192
	global_load_dwordx4 v[242:245], v[84:85], off offset:192
	s_ashr_i32 s17, s16, 31
	v_readlane_b32 s36, v253, 11
	v_readlane_b32 s37, v253, 12
	v_lshlrev_b32_e32 v114, 14, v91
	v_or_b32_e32 v99, 16, v91
	s_waitcnt vmcnt(31) lgkmcnt(1)
	v_mfma_f32_16x16x32_bf16 v[2:5], v[6:9], v[26:29], 0
	s_waitcnt lgkmcnt(0)
	v_mfma_f32_16x16x32_bf16 v[6:9], v[6:9], v[30:33], 0
	s_waitcnt vmcnt(30)
	v_mfma_f32_16x16x32_bf16 v[10:13], v[26:29], v[14:17], 0
	v_mfma_f32_16x16x32_bf16 v[14:17], v[30:33], v[14:17], 0
	s_waitcnt vmcnt(29)
	v_mfma_f32_16x16x32_bf16 v[42:45], v[34:37], v[26:29], 0
	v_mfma_f32_16x16x32_bf16 v[34:37], v[34:37], v[30:33], 0
	s_waitcnt vmcnt(28)
	v_mfma_f32_16x16x32_bf16 v[46:49], v[26:29], v[38:41], 0
	v_mfma_f32_16x16x32_bf16 v[38:41], v[30:33], v[38:41], 0
	s_waitcnt vmcnt(27)
	v_mfma_f32_16x16x32_bf16 v[62:65], v[50:53], v[26:29], 0
	v_mfma_f32_16x16x32_bf16 v[50:53], v[50:53], v[30:33], 0
	s_waitcnt vmcnt(26)
	v_mfma_f32_16x16x32_bf16 v[66:69], v[26:29], v[54:57], 0
	v_mfma_f32_16x16x32_bf16 v[54:57], v[30:33], v[54:57], 0
	s_waitcnt vmcnt(25)
	v_mfma_f32_16x16x32_bf16 v[100:103], v[70:73], v[26:29], 0
	v_mfma_f32_16x16x32_bf16 v[70:73], v[70:73], v[30:33], 0
	s_waitcnt vmcnt(24)
	v_mfma_f32_16x16x32_bf16 v[26:29], v[26:29], v[74:77], 0
	v_mfma_f32_16x16x32_bf16 v[30:33], v[30:33], v[74:77], 0
	ds_read_b128 v[74:77], v89 offset:12864
	ds_read_b128 v[104:107], v89 offset:17216
	s_waitcnt vmcnt(23) lgkmcnt(1)
	v_mfma_f32_16x16x32_bf16 v[2:5], v[140:143], v[74:77], v[2:5]
	s_waitcnt lgkmcnt(0)
	v_mfma_f32_16x16x32_bf16 v[6:9], v[140:143], v[104:107], v[6:9]
	s_waitcnt vmcnt(22)
	v_mfma_f32_16x16x32_bf16 v[10:13], v[74:77], v[144:147], v[10:13]
	v_mfma_f32_16x16x32_bf16 v[14:17], v[104:107], v[144:147], v[14:17]
	s_waitcnt vmcnt(21)
	v_mfma_f32_16x16x32_bf16 v[42:45], v[148:151], v[74:77], v[42:45]
	v_mfma_f32_16x16x32_bf16 v[34:37], v[148:151], v[104:107], v[34:37]
	s_waitcnt vmcnt(20)
	v_mfma_f32_16x16x32_bf16 v[46:49], v[74:77], v[152:155], v[46:49]
	v_mfma_f32_16x16x32_bf16 v[38:41], v[104:107], v[152:155], v[38:41]
	s_waitcnt vmcnt(19)
	v_mfma_f32_16x16x32_bf16 v[62:65], v[156:159], v[74:77], v[62:65]
	v_mfma_f32_16x16x32_bf16 v[50:53], v[156:159], v[104:107], v[50:53]
	s_waitcnt vmcnt(18)
	v_mfma_f32_16x16x32_bf16 v[66:69], v[74:77], v[160:163], v[66:69]
	v_mfma_f32_16x16x32_bf16 v[54:57], v[104:107], v[160:163], v[54:57]
	s_waitcnt vmcnt(17)
	v_mfma_f32_16x16x32_bf16 v[100:103], v[164:167], v[74:77], v[100:103]
	v_mfma_f32_16x16x32_bf16 v[70:73], v[164:167], v[104:107], v[70:73]
	s_waitcnt vmcnt(16)
	v_mfma_f32_16x16x32_bf16 v[74:77], v[74:77], v[168:171], v[26:29]
	v_mfma_f32_16x16x32_bf16 v[104:107], v[104:107], v[168:171], v[30:33]
	ds_read_b128 v[108:111], v89 offset:12928
	ds_read_b128 v[116:119], v89 offset:17280
	s_waitcnt vmcnt(14) lgkmcnt(1)
	v_mfma_f32_16x16x32_bf16 v[120:123], v[108:111], v[176:179], v[10:13]
	s_waitcnt lgkmcnt(0)
	v_mfma_f32_16x16x32_bf16 v[124:127], v[116:119], v[176:179], v[14:17]
	s_nop 0
	s_nop 0
	s_waitcnt vmcnt(12)
	v_mfma_f32_16x16x32_bf16 v[46:49], v[108:111], v[184:187], v[46:49]
	v_mfma_f32_16x16x32_bf16 v[136:139], v[116:119], v[184:187], v[38:41]
	v_mfma_f32_16x16x32_bf16 v[128:131], v[180:183], v[108:111], v[42:45]
	v_mfma_f32_16x16x32_bf16 v[132:135], v[180:183], v[116:119], v[34:37]
	s_waitcnt vmcnt(11)
	v_mfma_f32_16x16x32_bf16 v[10:13], v[188:191], v[108:111], v[62:65]
	s_waitcnt vmcnt(10)
	v_mfma_f32_16x16x32_bf16 v[42:45], v[108:111], v[192:195], v[66:69]
	v_mfma_f32_16x16x32_bf16 v[62:65], v[116:119], v[192:195], v[54:57]
	v_mfma_f32_16x16x32_bf16 v[2:5], v[172:175], v[108:111], v[2:5]
	v_mfma_f32_16x16x32_bf16 v[6:9], v[172:175], v[116:119], v[6:9]
	v_mfma_f32_16x16x32_bf16 v[26:29], v[188:191], v[116:119], v[50:53]
	s_waitcnt vmcnt(9)
	v_mfma_f32_16x16x32_bf16 v[14:17], v[196:199], v[108:111], v[100:103]
	v_mfma_f32_16x16x32_bf16 v[30:33], v[196:199], v[116:119], v[70:73]
	s_waitcnt vmcnt(8)
	v_mfma_f32_16x16x32_bf16 v[38:41], v[108:111], v[200:203], v[74:77]
	s_nop 0
	ds_read_b128 v[70:73], v89 offset:12992
	s_nop 0
	ds_read_b128 v[74:77], v89 offset:17344
	v_mfma_f32_16x16x32_bf16 v[66:69], v[116:119], v[200:203], v[104:107]
	s_waitcnt vmcnt(7) lgkmcnt(0)
	v_mfma_f32_16x16x32_bf16 v[18:21], v[204:207], v[74:77], v[6:9]
	s_nop 2
	v_mfma_f32_16x16x32_bf16 v[50:53], v[204:207], v[70:73], v[2:5]
	s_waitcnt vmcnt(6)
	v_mfma_f32_16x16x32_bf16 v[34:37], v[70:73], v[208:211], v[120:123]
	v_mfma_f32_16x16x32_bf16 v[2:5], v[74:77], v[208:211], v[124:127]
	s_waitcnt vmcnt(5)
	v_mfma_f32_16x16x32_bf16 v[54:57], v[212:215], v[70:73], v[128:131]
	s_nop 4
	v_cvt_pk_bf16_f32 v34, v34, v35
	v_cvt_pk_bf16_f32 v35, v36, v37
	v_cvt_pk_bf16_f32 v2, v2, v3
	v_mfma_f32_16x16x32_bf16 v[22:25], v[212:215], v[74:77], v[132:135]
	v_cvt_pk_bf16_f32 v3, v4, v5
	s_waitcnt vmcnt(4)
	v_mfma_f32_16x16x32_bf16 v[46:49], v[70:73], v[216:219], v[46:49]
	v_mfma_f32_16x16x32_bf16 v[6:9], v[74:77], v[216:219], v[136:139]
	s_nop 4
	v_cvt_pk_bf16_f32 v46, v46, v47
	v_cvt_pk_bf16_f32 v47, v48, v49
	s_waitcnt vmcnt(3)
	v_mfma_f32_16x16x32_bf16 v[58:61], v[220:223], v[70:73], v[10:13]
	v_mfma_f32_16x16x32_bf16 v[26:29], v[220:223], v[74:77], v[26:29]
	s_nop 0
	s_waitcnt vmcnt(2)
	v_mfma_f32_16x16x32_bf16 v[10:13], v[74:77], v[234:237], v[62:65]
	s_waitcnt vmcnt(1)
	v_mfma_f32_16x16x32_bf16 v[62:65], v[238:241], v[70:73], v[14:17]
	v_mfma_f32_16x16x32_bf16 v[30:33], v[238:241], v[74:77], v[30:33]
	v_lshl_add_u32 v103, v91, 7, 0
	v_lshlrev_b32_e32 v102, 5, v88
	s_waitcnt vmcnt(0)
	v_mfma_f32_16x16x32_bf16 v[14:17], v[74:77], v[242:245], v[66:69]
	v_mul_f32_e32 v76, v51, v51
	v_fmac_f32_e32 v76, v50, v50
	v_fmac_f32_e32 v76, v52, v52
	v_fmac_f32_e32 v76, v53, v53
	v_fmac_f32_e32 v76, v54, v54
	v_fmac_f32_e32 v76, v55, v55
	v_fmac_f32_e32 v76, v56, v56
	v_fmac_f32_e32 v76, v57, v57
	v_fmac_f32_e32 v76, v58, v58
	v_fmac_f32_e32 v76, v59, v59
	v_fmac_f32_e32 v76, v60, v60
	v_mfma_f32_16x16x32_bf16 v[42:45], v[70:73], v[234:237], v[42:45]
	v_fmac_f32_e32 v76, v61, v61
	v_add_u32_e32 v104, v103, v102
	v_fmac_f32_e32 v76, v62, v62
	v_mfma_f32_16x16x32_bf16 v[38:41], v[70:73], v[242:245], v[38:41]
	ds_read_b128 v[86:89], v104 offset:21504
	ds_read_b128 v[106:109], v104 offset:21520
	v_fmac_f32_e32 v76, v63, v63
	v_fmac_f32_e32 v76, v64, v64
	v_fmac_f32_e32 v76, v65, v65
	s_waitcnt lgkmcnt(1)
	v_fmac_f32_e32 v76, v86, v86
	v_fmac_f32_e32 v76, v87, v87
	v_pk_mul_f32 v[68:69], v[88:89], v[88:89]
	v_cndmask_b32_e64 v66, v228, v98, s[0:1]
	v_add_f32_e32 v68, v68, v76
	v_add_f32_e32 v76, v69, v68
	s_waitcnt lgkmcnt(0)
	v_pk_mul_f32 v[68:69], v[106:107], v[106:107]
	v_lshlrev_b32_e32 v100, 2, v66
	v_add_f32_e32 v68, v68, v76
	v_add_f32_e32 v76, v69, v68
	v_pk_mul_f32 v[68:69], v[108:109], v[108:109]
	s_lshl_b32 s0, s2, 2
	v_add_f32_e32 v68, v68, v76
	v_add_f32_e32 v68, v69, v68
	ds_bpermute_b32 v69, v100, v68
	s_add_i32 s0, s3, s0
	s_ashr_i32 s1, s0, 31
	v_cndmask_b32_e32 v66, v228, v97, vcc
	s_lshl_b64 s[18:19], s[0:1], 13
	v_lshlrev_b32_e32 v101, 2, v66
	s_add_u32 s18, s18, s16
	s_waitcnt lgkmcnt(0)
	v_add_f32_e32 v68, v68, v69
	s_addc_u32 s3, s19, s17
	s_lshl_b64 s[0:1], s[0:1], 20
	v_readlane_b32 s19, v253, 17
	ds_bpermute_b32 v69, v101, v68
	s_add_u32 s19, s19, s0
	v_readlane_b32 s0, v253, 18
	s_addc_u32 s38, s0, s1
	s_lshl_b64 s[0:1], s[16:17], 1
	s_add_u32 s0, s19, s0
	s_addc_u32 s1, s38, s1
	v_lshlrev_b64 v[84:85], 1, v[78:79]
	v_lshl_add_u64 v[70:71], s[0:1], 0, v[84:85]
	s_waitcnt lgkmcnt(0)
	v_add_f32_e32 v68, v68, v69
	v_readlane_b32 s0, v253, 15
	v_fmamk_f32 v68, v68, 0x3c2aaaab, v225
	v_readlane_b32 s1, v253, 16
	v_lshlrev_b64 v[66:67], 2, v[78:79]
	v_rsq_f32_e32 v90, v68
	v_or_b32_e32 v68, s18, v91
	v_mov_b64_e32 v[86:87], s[0:1]
	v_lshl_add_u64 v[72:73], s[36:37], 0, v[66:67]
	v_readlane_b32 s36, v253, 13
	v_mad_u64_u32 v[68:69], s[0:1], v68, s8, v[86:87]
	v_mov_b32_e32 v108, 0xc0
	v_readlane_b32 s37, v253, 14
	v_mad_i32_i24 v69, s3, v108, v69
	v_lshl_add_u64 v[76:77], s[22:23], 0, v[66:67]
	v_lshl_add_u64 v[74:75], s[36:37], 0, v[66:67]
	v_lshl_add_u64 v[88:89], v[68:69], 0, v[84:85]
	global_load_dwordx4 v[212:215], v[76:77], off offset:64
	global_load_dwordx4 v[216:219], v[76:77], off offset:128
	global_load_dwordx4 v[220:223], v[76:77], off offset:192
	global_load_dwordx4 v[66:69], v[76:77], off
	v_pk_mul_f32 v[50:51], v[50:51], v[90:91] op_sel_hi:[1,0]
	v_pk_mul_f32 v[52:53], v[52:53], v[90:91] op_sel_hi:[1,0]
	v_pk_mul_f32 v[54:55], v[54:55], v[90:91] op_sel_hi:[1,0]
	v_lshl_add_u64 v[36:37], v[70:71], 0, v[114:115]
	v_cvt_pk_bf16_f32 v38, v38, v39
	v_cvt_pk_bf16_f32 v39, v40, v41
	s_waitcnt vmcnt(0)
	v_pk_mul_f32 v[50:51], v[66:67], v[50:51]
	v_pk_mul_f32 v[52:53], v[68:69], v[52:53]
	v_cvt_pk_bf16_f32 v50, v50, v51
	v_cvt_pk_bf16_f32 v51, v52, v53
	global_store_dwordx2 v[88:89], v[50:51], off
	v_sub_u32_e32 v66, v104, v92
	ds_read_b128 v[66:69], v66 offset:21568
	v_pk_mul_f32 v[50:51], v[212:213], v[54:55]
	v_pk_mul_f32 v[54:55], v[56:57], v[90:91] op_sel_hi:[1,0]
	v_cvt_pk_bf16_f32 v50, v50, v51
	v_pk_mul_f32 v[52:53], v[54:55], v[214:215]
	v_pk_mul_f32 v[54:55], v[58:59], v[90:91] op_sel_hi:[1,0]
	v_cvt_pk_bf16_f32 v51, v52, v53
	global_store_dwordx2 v[88:89], v[50:51], off offset:32
	v_add_u32_e32 v58, v103, v92
	v_pk_mul_f32 v[50:51], v[54:55], v[216:217]
	v_pk_mul_f32 v[54:55], v[60:61], v[90:91] op_sel_hi:[1,0]
	v_cvt_pk_bf16_f32 v50, v50, v51
	v_pk_mul_f32 v[52:53], v[54:55], v[218:219]
	v_pk_mul_f32 v[54:55], v[62:63], v[90:91] op_sel_hi:[1,0]
	v_cvt_pk_bf16_f32 v51, v52, v53
	global_store_dwordx2 v[88:89], v[50:51], off offset:64
	ds_read_b128 v[58:61], v58 offset:21504
	s_waitcnt lgkmcnt(0)
	v_pk_mul_f32 v[58:59], v[90:91], v[58:59] op_sel_hi:[0,1]
	v_pk_mul_f32 v[50:51], v[54:55], v[220:221]
	v_pk_mul_f32 v[54:55], v[64:65], v[90:91] op_sel_hi:[1,0]
	v_cvt_pk_bf16_f32 v50, v50, v51
	v_pk_mul_f32 v[52:53], v[54:55], v[222:223]
	v_lshlrev_b64 v[54:55], 6, v[80:81]
	v_cvt_pk_bf16_f32 v51, v52, v53
	global_store_dwordx2 v[88:89], v[50:51], off offset:96
	global_load_dwordx4 v[62:65], v[76:77], off offset:256
	global_load_dwordx4 v[104:107], v[76:77], off offset:320
	v_lshl_add_u64 v[50:51], v[72:73], 0, v[54:55]
	v_lshl_add_u64 v[54:55], v[74:75], 0, v[54:55]
	global_load_dwordx4 v[50:53], v[50:51], off
	s_waitcnt vmcnt(2)
	v_pk_mul_f32 v[58:59], v[58:59], v[62:63]
	global_load_dwordx4 v[54:57], v[54:55], off
	v_pk_mul_f32 v[62:63], v[90:91], v[66:67] op_sel_hi:[0,1]
	s_waitcnt vmcnt(2)
	v_pk_mul_f32 v[62:63], v[62:63], v[104:105]
	s_waitcnt vmcnt(0)
	v_pk_mul_f32 v[66:67], v[54:55], v[62:63]
	s_nop 0
	v_pk_fma_f32 v[66:67], v[50:51], v[58:59], v[66:67] neg_lo:[0,0,1] neg_hi:[0,0,1]
	v_pk_mul_f32 v[50:51], v[50:51], v[62:63]
	s_nop 0
	v_pk_fma_f32 v[50:51], v[54:55], v[58:59], v[50:51]
	v_pk_mul_f32 v[58:59], v[90:91], v[68:69] op_sel_hi:[0,1]
	v_pk_mul_f32 v[54:55], v[90:91], v[60:61] op_sel_hi:[0,1]
	v_pk_mul_f32 v[58:59], v[58:59], v[106:107]
	v_pk_mul_f32 v[54:55], v[54:55], v[64:65]
	v_pk_mul_f32 v[60:61], v[56:57], v[58:59]
	v_cvt_pk_bf16_f32 v50, v50, v51
	v_pk_fma_f32 v[60:61], v[52:53], v[54:55], v[60:61] neg_lo:[0,0,1] neg_hi:[0,0,1]
	v_pk_mul_f32 v[52:53], v[52:53], v[58:59]
	s_nop 0
	v_pk_fma_f32 v[52:53], v[56:57], v[54:55], v[52:53]
	v_cvt_pk_bf16_f32 v54, v66, v67
	v_cvt_pk_bf16_f32 v55, v60, v61
	v_cvt_pk_bf16_f32 v51, v52, v53
	global_store_dwordx2 v[88:89], v[54:55], off offset:128
	global_store_dwordx2 v[88:89], v[50:51], off offset:160
	global_store_dwordx2 v[36:37], v[34:35], off
	v_or_b32_e32 v34, 0x40000, v114
	v_mov_b32_e32 v35, v115
	v_lshl_add_u64 v[48:49], v[70:71], 0, v[34:35]
	global_store_dwordx2 v[48:49], v[46:47], off
	v_cvt_pk_bf16_f32 v46, v42, v43
	v_or_b32_e32 v42, 0x80000, v114
	v_or_b32_e32 v114, 0xc0000, v114
	v_lshl_add_u64 v[40:41], v[70:71], 0, v[114:115]
	global_store_dwordx2 v[40:41], v[38:39], off
	v_mul_f32_e32 v40, v19, v19
	v_fmac_f32_e32 v40, v18, v18
	v_fmac_f32_e32 v40, v20, v20
	v_fmac_f32_e32 v40, v21, v21
	v_fmac_f32_e32 v40, v22, v22
	v_fmac_f32_e32 v40, v23, v23
	v_fmac_f32_e32 v40, v24, v24
	v_fmac_f32_e32 v40, v25, v25
	v_fmac_f32_e32 v40, v26, v26
	v_mov_b32_e32 v43, v115
	v_fmac_f32_e32 v40, v27, v27
	v_cvt_pk_bf16_f32 v47, v44, v45
	v_lshl_add_u64 v[44:45], v[70:71], 0, v[42:43]
	v_fmac_f32_e32 v40, v28, v28
	v_lshlrev_b32_e32 v38, 7, v99
	global_store_dwordx2 v[44:45], v[46:47], off
	v_fmac_f32_e32 v40, v29, v29
	v_add3_u32 v41, 0, v38, v102
	v_fmac_f32_e32 v40, v30, v30
	ds_read_b128 v[44:47], v41 offset:21504
	ds_read_b128 v[48:51], v41 offset:21520
	v_fmac_f32_e32 v40, v31, v31
	v_fmac_f32_e32 v40, v32, v32
	v_fmac_f32_e32 v40, v33, v33
	s_waitcnt lgkmcnt(1)
	v_fmac_f32_e32 v40, v44, v44
	v_fmac_f32_e32 v40, v45, v45
	v_pk_mul_f32 v[38:39], v[46:47], v[46:47]
	global_load_dwordx4 v[212:215], v[76:77], off offset:64
	global_load_dwordx4 v[216:219], v[76:77], off offset:128
	global_load_dwordx4 v[220:223], v[76:77], off offset:192
	global_load_dwordx4 v[44:47], v[76:77], off
	v_add_f32_e32 v38, v40, v38
	v_add_f32_e32 v40, v38, v39
	s_waitcnt lgkmcnt(0)
	v_pk_mul_f32 v[38:39], v[48:49], v[48:49]
	s_nop 0
	v_add_f32_e32 v38, v40, v38
	v_add_f32_e32 v40, v38, v39
	v_pk_mul_f32 v[38:39], v[50:51], v[50:51]
	s_nop 0
	v_add_f32_e32 v38, v40, v38
	v_add_f32_e32 v38, v38, v39
	ds_bpermute_b32 v39, v100, v38
	s_waitcnt lgkmcnt(0)
	v_add_f32_e32 v38, v38, v39
	ds_bpermute_b32 v39, v101, v38
	s_waitcnt lgkmcnt(0)
	v_add_f32_e32 v38, v38, v39
	v_fmamk_f32 v38, v38, 0x3c2aaaab, v225
	v_rsq_f32_e32 v40, v38
	v_or_b32_e32 v38, s18, v99
	v_mad_u64_u32 v[38:39], s[0:1], v38, s8, v[86:87]
	v_pk_mul_f32 v[18:19], v[18:19], v[40:41] op_sel_hi:[1,0]
	v_pk_mul_f32 v[20:21], v[20:21], v[40:41] op_sel_hi:[1,0]
	v_mad_i32_i24 v39, s3, v108, v39
	v_lshl_add_u64 v[38:39], v[38:39], 0, v[84:85]
	v_pk_mul_f32 v[22:23], v[22:23], v[40:41] op_sel_hi:[1,0]
	s_mov_b64 s[18:19], 0
	s_waitcnt vmcnt(0)
	v_pk_mul_f32 v[18:19], v[44:45], v[18:19]
	v_pk_mul_f32 v[20:21], v[46:47], v[20:21]
	v_cvt_pk_bf16_f32 v18, v18, v19
	v_cvt_pk_bf16_f32 v19, v20, v21
	global_store_dwordx2 v[38:39], v[18:19], off
	v_pk_mul_f32 v[18:19], v[212:213], v[22:23]
	v_pk_mul_f32 v[22:23], v[24:25], v[40:41] op_sel_hi:[1,0]
	v_cvt_pk_bf16_f32 v18, v18, v19
	v_pk_mul_f32 v[20:21], v[22:23], v[214:215]
	v_pk_mul_f32 v[22:23], v[26:27], v[40:41] op_sel_hi:[1,0]
	v_cvt_pk_bf16_f32 v19, v20, v21
	global_store_dwordx2 v[38:39], v[18:19], off offset:32
	v_pk_mul_f32 v[18:19], v[22:23], v[216:217]
	v_pk_mul_f32 v[22:23], v[28:29], v[40:41] op_sel_hi:[1,0]
	v_cvt_pk_bf16_f32 v18, v18, v19
	v_pk_mul_f32 v[20:21], v[22:23], v[218:219]
	v_pk_mul_f32 v[22:23], v[30:31], v[40:41] op_sel_hi:[1,0]
	v_cvt_pk_bf16_f32 v19, v20, v21
	global_store_dwordx2 v[38:39], v[18:19], off offset:64
	v_pk_mul_f32 v[18:19], v[22:23], v[220:221]
	v_pk_mul_f32 v[22:23], v[32:33], v[40:41] op_sel_hi:[1,0]
	v_cvt_pk_bf16_f32 v18, v18, v19
	v_pk_mul_f32 v[20:21], v[22:23], v[222:223]
	v_sub_u32_e32 v41, v41, v92
	v_cvt_pk_bf16_f32 v19, v20, v21
	global_store_dwordx2 v[38:39], v[18:19], off offset:96
	v_or_b32_e32 v18, s90, v99
	v_ashrrev_i32_e32 v19, 31, v18
	v_lshlrev_b64 v[22:23], 6, v[18:19]
	global_load_dwordx4 v[30:33], v[76:77], off offset:256
	global_load_dwordx4 v[48:51], v[76:77], off offset:320
	v_lshl_add_u64 v[18:19], v[72:73], 0, v[22:23]
	v_lshl_add_u64 v[22:23], v[74:75], 0, v[22:23]
	global_load_dwordx4 v[18:21], v[18:19], off
	ds_read_b128 v[26:29], v41 offset:21504
	ds_read_b128 v[44:47], v41 offset:21568
	global_load_dwordx4 v[22:25], v[22:23], off
	s_waitcnt lgkmcnt(1)
	v_pk_mul_f32 v[26:27], v[40:41], v[26:27] op_sel_hi:[0,1]
	s_waitcnt vmcnt(3)
	v_pk_mul_f32 v[26:27], v[26:27], v[30:31]
	s_waitcnt lgkmcnt(0)
	v_pk_mul_f32 v[30:31], v[40:41], v[44:45] op_sel_hi:[0,1]
	s_waitcnt vmcnt(2)
	v_pk_mul_f32 v[30:31], v[30:31], v[48:49]
	s_waitcnt vmcnt(0)
	v_pk_mul_f32 v[44:45], v[22:23], v[30:31]
	s_nop 0
	v_pk_fma_f32 v[44:45], v[18:19], v[26:27], v[44:45] neg_lo:[0,0,1] neg_hi:[0,0,1]
	v_pk_mul_f32 v[18:19], v[18:19], v[30:31]
	s_nop 0
	v_pk_fma_f32 v[18:19], v[22:23], v[26:27], v[18:19]
	v_pk_mul_f32 v[26:27], v[40:41], v[46:47] op_sel_hi:[0,1]
	v_pk_mul_f32 v[22:23], v[40:41], v[28:29] op_sel_hi:[0,1]
	v_pk_mul_f32 v[26:27], v[26:27], v[50:51]
	v_pk_mul_f32 v[22:23], v[22:23], v[32:33]
	v_pk_mul_f32 v[28:29], v[24:25], v[26:27]
	v_cvt_pk_bf16_f32 v18, v18, v19
	v_pk_fma_f32 v[28:29], v[20:21], v[22:23], v[28:29] neg_lo:[0,0,1] neg_hi:[0,0,1]
	v_pk_mul_f32 v[20:21], v[20:21], v[26:27]
	s_nop 0
	v_pk_fma_f32 v[20:21], v[24:25], v[22:23], v[20:21]
	v_cvt_pk_bf16_f32 v22, v44, v45
	v_cvt_pk_bf16_f32 v19, v20, v21
	v_cvt_pk_bf16_f32 v23, v28, v29
	global_store_dwordx2 v[38:39], v[18:19], off offset:160
	v_lshl_add_u64 v[18:19], v[70:71], 0, 32
	global_store_dwordx2 v[38:39], v[22:23], off offset:128
	global_store_dwordx2 v[36:37], v[2:3], off offset:32
	v_cvt_pk_bf16_f32 v2, v6, v7
	v_cvt_pk_bf16_f32 v3, v8, v9
	v_lshl_add_u64 v[4:5], v[18:19], 0, v[34:35]
	global_store_dwordx2 v[4:5], v[2:3], off
	v_cvt_pk_bf16_f32 v2, v10, v11
	v_cvt_pk_bf16_f32 v3, v12, v13
	v_lshl_add_u64 v[4:5], v[18:19], 0, v[42:43]
	global_store_dwordx2 v[4:5], v[2:3], off
	v_cvt_pk_bf16_f32 v2, v14, v15
	v_cvt_pk_bf16_f32 v3, v16, v17
	v_lshl_add_u64 v[4:5], v[18:19], 0, v[114:115]
	global_store_dwordx2 v[4:5], v[2:3], off
.LBB0_402:
	s_andn2_b64 vcc, exec, s[18:19]
	s_cbranch_vccnz .LBB0_404
	s_mul_i32 s0, s91, 0x60
	s_mul_i32 s1, s91, 0x9000
	s_mul_hi_i32 s3, s0, 0x180
	s_add_u32 s0, s26, s1
	s_addc_u32 s1, s88, s3
	v_mul_u32_u24_e32 v2, 0xc0, v91
	v_mul_u32_u24_e32 v3, 0xc8, v91
	v_lshl_add_u64 v[36:37], v[82:83], 1, s[0:1]
	v_lshlrev_b32_e32 v3, 1, v3
	v_lshlrev_b32_e32 v114, 1, v2
	v_add3_u32 v88, 0, v92, v3
	v_lshl_add_u64 v[2:3], v[36:37], 0, v[114:115]
	s_mov_b64 s[0:1], 0x1800
	v_lshl_add_u64 v[38:39], v[2:3], 0, s[0:1]
	s_movk_i32 s0, 0x1000
	v_add_co_u32_e32 v20, vcc, s0, v2
	s_movk_i32 s0, 0x3000
	s_nop 0
	v_addc_co_u32_e32 v21, vcc, 0, v3, vcc
	v_add_co_u32_e32 v64, vcc, s0, v2
	s_movk_i32 s0, 0x4000
	s_nop 0
	v_addc_co_u32_e32 v65, vcc, 0, v3, vcc
	v_add_co_u32_e32 v62, vcc, s0, v2
	s_movk_i32 s0, 0x7000
	s_nop 0
	v_addc_co_u32_e32 v63, vcc, 0, v3, vcc
	v_or_b32_e32 v114, 0x6000, v114
	v_add_co_u32_e32 v68, vcc, s0, v2
	v_lshl_add_u64 v[66:67], v[36:37], 0, v[114:115]
	s_nop 0
	v_addc_co_u32_e32 v69, vcc, 0, v3, vcc
	ds_read_b128 v[4:7], v88
	ds_read_b128 v[8:11], v88 offset:6400
	global_load_dwordx4 v[12:15], v[2:3], off
	global_load_dwordx4 v[28:31], v[64:65], off
	global_load_dwordx4 v[40:43], v[62:63], off offset:2048
	global_load_dwordx4 v[48:51], v[66:67], off
	global_load_dwordx4 v[56:59], v[68:69], off offset:2048
	v_cmp_lt_i32_e32 vcc, v98, v96
	global_load_dwordx4 v[20:23], v[20:21], off offset:2048
	global_load_dwordx4 v[140:143], v[2:3], off offset:64
	global_load_dwordx4 v[144:147], v[38:39], off offset:64
	global_load_dwordx4 v[148:151], v[64:65], off offset:64
	global_load_dwordx4 v[152:155], v[62:63], off offset:2112
	global_load_dwordx4 v[156:159], v[66:67], off offset:64
	global_load_dwordx4 v[160:163], v[68:69], off offset:2112
	global_load_dwordx4 v[164:167], v[2:3], off offset:128
	global_load_dwordx4 v[168:171], v[38:39], off offset:128
	global_load_dwordx4 v[172:175], v[64:65], off offset:128
	global_load_dwordx4 v[176:179], v[62:63], off offset:2176
	global_load_dwordx4 v[180:183], v[66:67], off offset:128
	global_load_dwordx4 v[184:187], v[68:69], off offset:2176
	global_load_dwordx4 v[188:191], v[2:3], off offset:192
	global_load_dwordx4 v[192:195], v[38:39], off offset:192
	global_load_dwordx4 v[196:199], v[64:65], off offset:192
	global_load_dwordx4 v[200:203], v[62:63], off offset:2240
	global_load_dwordx4 v[204:207], v[66:67], off offset:192
	global_load_dwordx4 v[208:211], v[68:69], off offset:2240
	global_load_dwordx4 v[212:215], v[2:3], off offset:256
	global_load_dwordx4 v[216:219], v[38:39], off offset:256
	global_load_dwordx4 v[220:223], v[66:67], off offset:256
	global_load_dwordx4 v[234:237], v[64:65], off offset:256
	global_load_dwordx4 v[238:241], v[62:63], off offset:2304
	global_load_dwordx4 v[242:245], v[68:69], off offset:2304
	s_lshl_b32 s0, s2, 2
	s_add_i32 s0, s91, s0
	s_ashr_i32 s1, s0, 31
	s_ashr_i32 s2, s16, 31
	s_lshl_b64 s[0:1], s[0:1], 13
	s_waitcnt vmcnt(29) lgkmcnt(1)
	v_mfma_f32_16x16x32_bf16 v[16:19], v[12:15], v[4:7], 0
	s_waitcnt lgkmcnt(0)
	v_mfma_f32_16x16x32_bf16 v[12:15], v[12:15], v[8:11], 0
	s_waitcnt vmcnt(24)
	v_mfma_f32_16x16x32_bf16 v[24:27], v[20:23], v[4:7], 0
	v_mfma_f32_16x16x32_bf16 v[20:23], v[20:23], v[8:11], 0
	v_mfma_f32_16x16x32_bf16 v[32:35], v[28:31], v[4:7], 0
	v_mfma_f32_16x16x32_bf16 v[28:31], v[28:31], v[8:11], 0
	v_mfma_f32_16x16x32_bf16 v[44:47], v[40:43], v[4:7], 0
	v_mfma_f32_16x16x32_bf16 v[40:43], v[40:43], v[8:11], 0
	v_mfma_f32_16x16x32_bf16 v[52:55], v[48:51], v[4:7], 0
	v_mfma_f32_16x16x32_bf16 v[48:51], v[48:51], v[8:11], 0
	v_mfma_f32_16x16x32_bf16 v[4:7], v[56:59], v[4:7], 0
	v_mfma_f32_16x16x32_bf16 v[8:11], v[56:59], v[8:11], 0
	ds_read_b128 v[56:59], v88 offset:64
	ds_read_b128 v[70:73], v88 offset:6464
	s_waitcnt vmcnt(23) lgkmcnt(1)
	v_mfma_f32_16x16x32_bf16 v[16:19], v[140:143], v[56:59], v[16:19]
	s_waitcnt lgkmcnt(0)
	v_mfma_f32_16x16x32_bf16 v[12:15], v[140:143], v[70:73], v[12:15]
	s_waitcnt vmcnt(22)
	v_mfma_f32_16x16x32_bf16 v[24:27], v[144:147], v[56:59], v[24:27]
	v_mfma_f32_16x16x32_bf16 v[20:23], v[144:147], v[70:73], v[20:23]
	s_waitcnt vmcnt(21)
	v_mfma_f32_16x16x32_bf16 v[32:35], v[148:151], v[56:59], v[32:35]
	v_mfma_f32_16x16x32_bf16 v[28:31], v[148:151], v[70:73], v[28:31]
	s_waitcnt vmcnt(20)
	v_mfma_f32_16x16x32_bf16 v[44:47], v[152:155], v[56:59], v[44:47]
	v_mfma_f32_16x16x32_bf16 v[40:43], v[152:155], v[70:73], v[40:43]
	s_waitcnt vmcnt(19)
	v_mfma_f32_16x16x32_bf16 v[52:55], v[156:159], v[56:59], v[52:55]
	v_mfma_f32_16x16x32_bf16 v[48:51], v[156:159], v[70:73], v[48:51]
	s_waitcnt vmcnt(18)
	v_mfma_f32_16x16x32_bf16 v[4:7], v[160:163], v[56:59], v[4:7]
	v_mfma_f32_16x16x32_bf16 v[8:11], v[160:163], v[70:73], v[8:11]
	global_load_dwordx4 v[140:143], v[2:3], off offset:320
	global_load_dwordx4 v[144:147], v[38:39], off offset:320
	global_load_dwordx4 v[148:151], v[64:65], off offset:320
	global_load_dwordx4 v[152:155], v[62:63], off offset:2368
	global_load_dwordx4 v[156:159], v[66:67], off offset:320
	global_load_dwordx4 v[160:163], v[68:69], off offset:2368
	ds_read_b128 v[56:59], v88 offset:128
	ds_read_b128 v[70:73], v88 offset:6528
	s_waitcnt vmcnt(23) lgkmcnt(1)
	v_mfma_f32_16x16x32_bf16 v[16:19], v[164:167], v[56:59], v[16:19]
	s_waitcnt lgkmcnt(0)
	v_mfma_f32_16x16x32_bf16 v[12:15], v[164:167], v[70:73], v[12:15]
	s_waitcnt vmcnt(22)
	v_mfma_f32_16x16x32_bf16 v[24:27], v[168:171], v[56:59], v[24:27]
	v_mfma_f32_16x16x32_bf16 v[20:23], v[168:171], v[70:73], v[20:23]
	s_waitcnt vmcnt(21)
	v_mfma_f32_16x16x32_bf16 v[32:35], v[172:175], v[56:59], v[32:35]
	v_mfma_f32_16x16x32_bf16 v[28:31], v[172:175], v[70:73], v[28:31]
	s_waitcnt vmcnt(20)
	v_mfma_f32_16x16x32_bf16 v[44:47], v[176:179], v[56:59], v[44:47]
	v_mfma_f32_16x16x32_bf16 v[40:43], v[176:179], v[70:73], v[40:43]
	s_waitcnt vmcnt(19)
	v_mfma_f32_16x16x32_bf16 v[52:55], v[180:183], v[56:59], v[52:55]
	v_mfma_f32_16x16x32_bf16 v[48:51], v[180:183], v[70:73], v[48:51]
	s_waitcnt vmcnt(18)
	v_mfma_f32_16x16x32_bf16 v[4:7], v[184:187], v[56:59], v[4:7]
	v_mfma_f32_16x16x32_bf16 v[8:11], v[184:187], v[70:73], v[8:11]
	ds_read_b128 v[56:59], v88 offset:192
	ds_read_b128 v[70:73], v88 offset:6592
	s_waitcnt vmcnt(17) lgkmcnt(1)
	v_mfma_f32_16x16x32_bf16 v[16:19], v[188:191], v[56:59], v[16:19]
	s_waitcnt lgkmcnt(0)
	v_mfma_f32_16x16x32_bf16 v[12:15], v[188:191], v[70:73], v[12:15]
	s_waitcnt vmcnt(16)
	v_mfma_f32_16x16x32_bf16 v[24:27], v[192:195], v[56:59], v[24:27]
	v_mfma_f32_16x16x32_bf16 v[20:23], v[192:195], v[70:73], v[20:23]
	s_waitcnt vmcnt(15)
	v_mfma_f32_16x16x32_bf16 v[32:35], v[196:199], v[56:59], v[32:35]
	v_mfma_f32_16x16x32_bf16 v[28:31], v[196:199], v[70:73], v[28:31]
	s_waitcnt vmcnt(14)
	v_mfma_f32_16x16x32_bf16 v[44:47], v[200:203], v[56:59], v[44:47]
	v_mfma_f32_16x16x32_bf16 v[40:43], v[200:203], v[70:73], v[40:43]
	s_waitcnt vmcnt(13)
	v_mfma_f32_16x16x32_bf16 v[84:87], v[204:207], v[56:59], v[52:55]
	s_nop 2
	ds_read_b128 v[100:103], v88 offset:256
	ds_read_b128 v[104:107], v88 offset:6656
	v_mfma_f32_16x16x32_bf16 v[48:51], v[204:207], v[70:73], v[48:51]
	s_waitcnt vmcnt(12)
	v_mfma_f32_16x16x32_bf16 v[74:77], v[208:211], v[56:59], v[4:7]
	s_nop 2
	s_waitcnt vmcnt(11) lgkmcnt(1)
	v_mfma_f32_16x16x32_bf16 v[108:111], v[212:215], v[100:103], v[16:19]
	s_waitcnt lgkmcnt(0)
	v_mfma_f32_16x16x32_bf16 v[116:119], v[212:215], v[104:107], v[12:15]
	v_mfma_f32_16x16x32_bf16 v[70:73], v[208:211], v[70:73], v[8:11]
	s_nop 2
	s_waitcnt vmcnt(10)
	v_mfma_f32_16x16x32_bf16 v[14:17], v[216:219], v[100:103], v[24:27]
	v_mfma_f32_16x16x32_bf16 v[58:61], v[216:219], v[104:107], v[20:23]
	s_waitcnt vmcnt(8)
	v_mfma_f32_16x16x32_bf16 v[22:25], v[234:237], v[100:103], v[32:35]
	v_mfma_f32_16x16x32_bf16 v[54:57], v[234:237], v[104:107], v[28:31]
	s_nop 1
	s_waitcnt vmcnt(7)
	v_mfma_f32_16x16x32_bf16 v[18:21], v[238:241], v[100:103], v[44:47]
	v_mfma_f32_16x16x32_bf16 v[26:29], v[238:241], v[104:107], v[40:43]
	v_mfma_f32_16x16x32_bf16 v[50:53], v[220:223], v[104:107], v[48:51]
	ds_read_b128 v[34:37], v88 offset:320
	s_nop 1
	ds_read_b128 v[46:49], v88 offset:6720
	s_waitcnt vmcnt(6)
	v_mfma_f32_16x16x32_bf16 v[42:45], v[242:245], v[104:107], v[70:73]
	s_nop 2
	s_waitcnt vmcnt(4) lgkmcnt(1)
	v_mfma_f32_16x16x32_bf16 v[38:41], v[144:147], v[34:37], v[14:17]
	s_waitcnt lgkmcnt(0)
	v_mfma_f32_16x16x32_bf16 v[14:17], v[144:147], v[46:49], v[58:61]
	s_nop 0
	s_waitcnt vmcnt(3)
	v_mfma_f32_16x16x32_bf16 v[58:61], v[148:151], v[34:37], v[22:25]
	v_mfma_f32_16x16x32_bf16 v[22:25], v[148:151], v[46:49], v[54:57]
	s_waitcnt vmcnt(2)
	v_mfma_f32_16x16x32_bf16 v[54:57], v[152:155], v[34:37], v[18:21]
	v_mfma_f32_16x16x32_bf16 v[18:21], v[152:155], v[46:49], v[26:29]
	v_mfma_f32_16x16x32_bf16 v[6:9], v[220:223], v[100:103], v[84:87]
	s_waitcnt vmcnt(1)
	v_mfma_f32_16x16x32_bf16 v[26:29], v[156:159], v[34:37], v[6:9]
	v_mfma_f32_16x16x32_bf16 v[6:9], v[156:159], v[46:49], v[50:53]
	s_nop 2
	v_mfma_f32_16x16x32_bf16 v[10:13], v[242:245], v[100:103], v[74:77]
	v_mfma_f32_16x16x32_bf16 v[30:33], v[140:143], v[34:37], v[108:111]
	v_mfma_f32_16x16x32_bf16 v[2:5], v[140:143], v[46:49], v[116:119]
	s_waitcnt vmcnt(0)
	v_mfma_f32_16x16x32_bf16 v[34:37], v[160:163], v[34:37], v[10:13]
	v_mfma_f32_16x16x32_bf16 v[10:13], v[160:163], v[46:49], v[42:45]
	s_nop 3
	v_mul_f32_e32 v46, v31, v31
	v_fmac_f32_e32 v46, v30, v30
	v_fmac_f32_e32 v46, v32, v32
	v_fmac_f32_e32 v46, v33, v33
	v_fmac_f32_e32 v46, v38, v38
	v_fmac_f32_e32 v46, v39, v39
	v_fmac_f32_e32 v46, v40, v40
	v_fmac_f32_e32 v46, v41, v41
	v_fmac_f32_e32 v46, v58, v58
	v_fmac_f32_e32 v46, v59, v59
	v_fmac_f32_e32 v46, v60, v60
	v_fmac_f32_e32 v46, v61, v61
	v_fmac_f32_e32 v46, v54, v54
	v_fmac_f32_e32 v46, v55, v55
	v_fmac_f32_e32 v46, v56, v56
	v_fmac_f32_e32 v46, v57, v57
	v_fmac_f32_e32 v46, v26, v26
	v_fmac_f32_e32 v46, v27, v27
	v_pk_mul_f32 v[44:45], v[28:29], v[28:29]
	v_cndmask_b32_e32 v42, v228, v98, vcc
	v_add_f32_e32 v44, v44, v46
	v_add_f32_e32 v48, v45, v44
	v_pk_mul_f32 v[46:47], v[34:35], v[34:35]
	v_pk_mul_f32 v[44:45], v[36:37], v[36:37]
	v_add_f32_e32 v46, v46, v48
	v_add_f32_e32 v46, v47, v46
	v_add_f32_e32 v44, v44, v46
	v_lshlrev_b32_e32 v69, 2, v42
	v_add_f32_e32 v44, v45, v44
	ds_bpermute_b32 v45, v69, v44
	v_cmp_lt_i32_e32 vcc, v97, v96
	v_mov_b32_e32 v43, s2
	s_waitcnt lgkmcnt(0)
	v_add_f32_e32 v44, v44, v45
	v_cndmask_b32_e32 v42, v228, v97, vcc
	v_lshlrev_b32_e32 v86, 2, v42
	ds_bpermute_b32 v45, v86, v44
	v_or_b32_e32 v42, s16, v91
	v_lshl_add_u64 v[64:65], v[42:43], 0, s[0:1]
	v_readlane_b32 s0, v253, 11
	v_lshlrev_b64 v[42:43], 2, v[78:79]
	s_waitcnt lgkmcnt(0)
	v_add_f32_e32 v44, v44, v45
	v_fmamk_f32 v44, v44, 0x3c2aaaab, v225
	v_rsq_f32_e32 v44, v44
	v_readlane_b32 s1, v253, 12
	v_lshl_add_u64 v[62:63], s[34:35], 0, v[42:43]
	global_load_dwordx4 v[212:215], v[62:63], off offset:64
	global_load_dwordx4 v[216:219], v[62:63], off offset:128
	global_load_dwordx4 v[220:223], v[62:63], off offset:192
	global_load_dwordx4 v[46:49], v[62:63], off offset:320
	v_lshl_add_u64 v[52:53], s[0:1], 0, v[42:43]
	v_readlane_b32 s0, v253, 13
	v_readlane_b32 s1, v253, 14
	v_mul_f32_e32 v68, 0x3e16c740, v44
	v_pk_mul_f32 v[30:31], v[30:31], v[68:69] op_sel_hi:[1,0]
	v_lshl_add_u64 v[50:51], s[0:1], 0, v[42:43]
	global_load_dwordx4 v[42:45], v[62:63], off
	v_pk_mul_f32 v[38:39], v[38:39], v[68:69] op_sel_hi:[1,0]
	v_pk_mul_f32 v[34:35], v[34:35], v[68:69] op_sel_hi:[1,0]
	v_pk_mul_f32 v[26:27], v[26:27], v[68:69] op_sel_hi:[1,0]
	v_readlane_b32 s0, v253, 19
	v_readlane_b32 s1, v253, 20
	s_waitcnt vmcnt(1)
	v_pk_mul_f32 v[34:35], v[34:35], v[46:47]
	v_lshl_add_u64 v[66:67], v[78:79], 1, s[0:1]
	s_waitcnt vmcnt(0)
	v_pk_mul_f32 v[72:73], v[42:43], v[30:31]
	v_pk_mul_f32 v[30:31], v[32:33], v[68:69] op_sel_hi:[1,0]
	s_nop 0
	v_pk_mul_f32 v[70:71], v[44:45], v[30:31]
	global_load_dwordx4 v[42:45], v[62:63], off offset:256
	s_waitcnt vmcnt(1)
	v_pk_mul_f32 v[76:77], v[212:213], v[38:39]
	v_pk_mul_f32 v[30:31], v[40:41], v[68:69] op_sel_hi:[1,0]
	v_pk_mul_f32 v[38:39], v[58:59], v[68:69] op_sel_hi:[1,0]
	v_pk_mul_f32 v[74:75], v[214:215], v[30:31]
	s_waitcnt vmcnt(0)
	v_pk_mul_f32 v[26:27], v[26:27], v[42:43]
	s_waitcnt vmcnt(0)
	v_pk_mul_f32 v[84:85], v[216:217], v[38:39]
	v_pk_mul_f32 v[30:31], v[60:61], v[68:69] op_sel_hi:[1,0]
	v_pk_mul_f32 v[38:39], v[54:55], v[68:69] op_sel_hi:[1,0]
	v_pk_mul_f32 v[58:59], v[218:219], v[30:31]
	s_waitcnt vmcnt(0)
	v_pk_mul_f32 v[60:61], v[220:221], v[38:39]
	v_pk_mul_f32 v[30:31], v[56:57], v[68:69] op_sel_hi:[1,0]
	v_lshlrev_b64 v[38:39], 6, v[80:81]
	v_pk_mul_f32 v[54:55], v[222:223], v[30:31]
	v_lshl_add_u64 v[30:31], v[52:53], 0, v[38:39]
	v_lshl_add_u64 v[38:39], v[50:51], 0, v[38:39]
	global_load_dwordx4 v[30:33], v[30:31], off
	s_nop 0
	global_load_dwordx4 v[38:41], v[38:39], off
	s_waitcnt vmcnt(0)
	v_pk_mul_f32 v[42:43], v[34:35], v[38:39]
	s_nop 0
	v_pk_fma_f32 v[42:43], v[26:27], v[30:31], v[42:43] neg_lo:[0,0,1] neg_hi:[0,0,1]
	v_pk_mul_f32 v[26:27], v[26:27], v[38:39]
	s_nop 0
	v_pk_fma_f32 v[30:31], v[34:35], v[30:31], v[26:27]
	v_pk_mul_f32 v[26:27], v[28:29], v[68:69] op_sel_hi:[1,0]
	v_pk_mul_f32 v[28:29], v[36:37], v[68:69] op_sel_hi:[1,0]
	v_pk_mul_f32 v[26:27], v[26:27], v[44:45]
	v_pk_mul_f32 v[28:29], v[28:29], v[48:49]
	v_cvt_pk_bf16_f32 v30, v30, v31
	v_pk_mul_f32 v[34:35], v[28:29], v[40:41]
	s_nop 0
	v_pk_fma_f32 v[34:35], v[26:27], v[32:33], v[34:35] neg_lo:[0,0,1] neg_hi:[0,0,1]
	v_pk_mul_f32 v[26:27], v[26:27], v[40:41]
	s_nop 0
	v_pk_fma_f32 v[28:29], v[28:29], v[32:33], v[26:27]
	v_mad_u64_u32 v[26:27], s[0:1], v64, s8, v[66:67]
	v_mad_i32_i24 v27, v65, s8, v27
	v_cvt_pk_bf16_f32 v31, v28, v29
	global_store_dwordx2 v[26:27], v[30:31], off offset:160
	v_mul_f32_e32 v30, v3, v3
	v_fmac_f32_e32 v30, v2, v2
	v_fmac_f32_e32 v30, v4, v4
	v_fmac_f32_e32 v30, v5, v5
	v_fmac_f32_e32 v30, v14, v14
	v_fmac_f32_e32 v30, v15, v15
	v_fmac_f32_e32 v30, v16, v16
	v_fmac_f32_e32 v30, v17, v17
	v_fmac_f32_e32 v30, v22, v22
	v_fmac_f32_e32 v30, v23, v23
	v_fmac_f32_e32 v30, v24, v24
	v_fmac_f32_e32 v30, v25, v25
	v_fmac_f32_e32 v30, v18, v18
	v_fmac_f32_e32 v30, v19, v19
	v_cvt_pk_bf16_f32 v32, v72, v73
	v_cvt_pk_bf16_f32 v33, v70, v71
	v_fmac_f32_e32 v30, v20, v20
	global_store_dwordx2 v[26:27], v[32:33], off
	v_cvt_pk_bf16_f32 v32, v76, v77
	v_cvt_pk_bf16_f32 v33, v74, v75
	v_fmac_f32_e32 v30, v21, v21
	global_store_dwordx2 v[26:27], v[32:33], off offset:32
	v_cvt_pk_bf16_f32 v32, v84, v85
	v_cvt_pk_bf16_f32 v33, v58, v59
	v_fmac_f32_e32 v30, v6, v6
	global_store_dwordx2 v[26:27], v[32:33], off offset:64
	v_cvt_pk_bf16_f32 v32, v60, v61
	v_cvt_pk_bf16_f32 v33, v54, v55
	v_fmac_f32_e32 v30, v7, v7
	v_pk_mul_f32 v[28:29], v[8:9], v[8:9]
	global_store_dwordx2 v[26:27], v[32:33], off offset:96
	v_cvt_pk_bf16_f32 v32, v42, v43
	v_cvt_pk_bf16_f32 v33, v34, v35
	v_add_f32_e32 v28, v28, v30
	global_store_dwordx2 v[26:27], v[32:33], off offset:128
	v_add_f32_e32 v32, v29, v28
	v_pk_mul_f32 v[30:31], v[10:11], v[10:11]
	v_pk_mul_f32 v[28:29], v[12:13], v[12:13]
	v_add_f32_e32 v30, v30, v32
	v_add_f32_e32 v30, v31, v30
	v_add_f32_e32 v28, v28, v30
	global_load_dwordx4 v[212:215], v[62:63], off offset:64
	global_load_dwordx4 v[216:219], v[62:63], off offset:128
	global_load_dwordx4 v[220:223], v[62:63], off offset:192
	global_load_dwordx4 v[30:33], v[62:63], off
	global_load_dwordx4 v[42:45], v[62:63], off offset:320
	v_add_f32_e32 v28, v29, v28
	ds_bpermute_b32 v29, v69, v28
	s_waitcnt lgkmcnt(0)
	v_add_f32_e32 v28, v28, v29
	ds_bpermute_b32 v29, v86, v28
	s_waitcnt lgkmcnt(0)
	v_add_f32_e32 v28, v28, v29
	v_fmamk_f32 v28, v28, 0x3c2aaaab, v225
	v_rsq_f32_e32 v28, v28
	s_nop 0
	v_mul_f32_e32 v28, 0x3e16c740, v28
	v_pk_mul_f32 v[2:3], v[2:3], v[28:29] op_sel_hi:[1,0]
	v_pk_mul_f32 v[14:15], v[14:15], v[28:29] op_sel_hi:[1,0]
	v_pk_mul_f32 v[10:11], v[10:11], v[28:29] op_sel_hi:[1,0]
	v_pk_mul_f32 v[6:7], v[6:7], v[28:29] op_sel_hi:[1,0]
	s_waitcnt vmcnt(1)
	v_pk_mul_f32 v[30:31], v[30:31], v[2:3]
	v_pk_mul_f32 v[2:3], v[4:5], v[28:29] op_sel_hi:[1,0]
	s_waitcnt vmcnt(0)
	v_pk_mul_f32 v[10:11], v[10:11], v[42:43]
	v_pk_mul_f32 v[32:33], v[32:33], v[2:3]
	s_waitcnt vmcnt(0)
	v_pk_mul_f32 v[34:35], v[212:213], v[14:15]
	v_pk_mul_f32 v[2:3], v[16:17], v[28:29] op_sel_hi:[1,0]
	v_pk_mul_f32 v[14:15], v[22:23], v[28:29] op_sel_hi:[1,0]
	v_pk_mul_f32 v[36:37], v[214:215], v[2:3]
	s_waitcnt vmcnt(0)
	v_pk_mul_f32 v[22:23], v[14:15], v[216:217]
	v_pk_mul_f32 v[2:3], v[24:25], v[28:29] op_sel_hi:[1,0]
	v_pk_mul_f32 v[14:15], v[18:19], v[28:29] op_sel_hi:[1,0]
	v_pk_mul_f32 v[24:25], v[2:3], v[218:219]
	s_waitcnt vmcnt(0)
	v_pk_mul_f32 v[38:39], v[14:15], v[220:221]
	v_pk_mul_f32 v[2:3], v[20:21], v[28:29] op_sel_hi:[1,0]
	global_load_dwordx4 v[18:21], v[62:63], off offset:256
	v_pk_mul_f32 v[40:41], v[2:3], v[222:223]
	v_or_b32_e32 v2, 16, v80
	v_ashrrev_i32_e32 v3, 31, v2
	v_lshlrev_b64 v[14:15], 6, v[2:3]
	v_lshl_add_u64 v[2:3], v[52:53], 0, v[14:15]
	v_lshl_add_u64 v[14:15], v[50:51], 0, v[14:15]
	global_load_dwordx4 v[2:5], v[2:3], off
	s_waitcnt vmcnt(1)
	v_pk_mul_f32 v[6:7], v[6:7], v[18:19]
	global_load_dwordx4 v[14:17], v[14:15], off
	s_waitcnt vmcnt(0)
	v_pk_mul_f32 v[18:19], v[10:11], v[14:15]
	s_nop 0
	v_pk_fma_f32 v[18:19], v[6:7], v[2:3], v[18:19] neg_lo:[0,0,1] neg_hi:[0,0,1]
	v_pk_mul_f32 v[6:7], v[6:7], v[14:15]
	s_nop 0
	v_pk_fma_f32 v[2:3], v[10:11], v[2:3], v[6:7]
	v_pk_mul_f32 v[6:7], v[8:9], v[28:29] op_sel_hi:[1,0]
	v_pk_mul_f32 v[8:9], v[12:13], v[28:29] op_sel_hi:[1,0]
	v_pk_mul_f32 v[6:7], v[6:7], v[20:21]
	v_pk_mul_f32 v[8:9], v[8:9], v[44:45]
	v_cvt_pk_bf16_f32 v2, v2, v3
	v_pk_mul_f32 v[10:11], v[8:9], v[16:17]
	s_nop 0
	v_pk_fma_f32 v[10:11], v[6:7], v[4:5], v[10:11] neg_lo:[0,0,1] neg_hi:[0,0,1]
	v_pk_mul_f32 v[6:7], v[6:7], v[16:17]
	s_nop 0
	v_pk_fma_f32 v[4:5], v[8:9], v[4:5], v[6:7]
	v_cvt_pk_bf16_f32 v6, v30, v31
	v_cvt_pk_bf16_f32 v7, v32, v33
	global_store_dwordx2 v[26:27], v[6:7], off offset:3072
	v_cvt_pk_bf16_f32 v6, v34, v35
	v_cvt_pk_bf16_f32 v7, v36, v37
	global_store_dwordx2 v[26:27], v[6:7], off offset:3104
	v_cvt_pk_bf16_f32 v6, v22, v23
	v_cvt_pk_bf16_f32 v7, v24, v25
	global_store_dwordx2 v[26:27], v[6:7], off offset:3136
	v_cvt_pk_bf16_f32 v6, v38, v39
	v_cvt_pk_bf16_f32 v7, v40, v41
	global_store_dwordx2 v[26:27], v[6:7], off offset:3168
	v_cvt_pk_bf16_f32 v6, v18, v19
	v_cvt_pk_bf16_f32 v7, v10, v11
	v_cvt_pk_bf16_f32 v3, v4, v5
	global_store_dwordx2 v[26:27], v[6:7], off offset:3200
	global_store_dwordx2 v[26:27], v[2:3], off offset:3232
